# v039 variant: only two P.V slots prefetched before the barrier, K address adds in the first MFMA gaps (softmax tail 8 instructions shorter)
# baseline (speedup 1.0000x reference)
; #define PK4(P, BASE, OUT) do { u32x4 w = {cvtpk(P[BASE + 0], P[BASE + 1]), cvtpk(P[BASE + 2], P[BASE + 3]), cvtpk(P[BASE + 4], P[BASE + 5]), cvtpk(P[BASE + 6], P[BASE + 7])}; \
;     OUT = *reinterpret_cast<bf16x8*>(&w); } while (0)
; __device__ __forceinline__ void smax_tile(f32x16& p0, f32x16& p1, float& mhat, float& l_reg, f32x16 (&o)[4], float* al_l, const bool first, int r32, int hi,
;                                           bf16x8& pa0, bf16x8& pa1, bf16x8& pa2, bf16x8& pa3) {
;     ...
; #pragma unroll
;     for (int r = 0; r < 16; ++r) p0[r] = __builtin_amdgcn_exp2f(p0[r]);
; #pragma unroll
;     for (int r = 0; r < 16; ++r) p1[r] = __builtin_amdgcn_exp2f(p1[r]);
;     float ps = p0[0];
; #pragma unroll
;     for (int r = 1; r < 16; ++r) ps += p0[r];
; #pragma unroll
;     for (int r = 0; r < 16; ++r) ps += p1[r];
;     { auto rr = __builtin_amdgcn_permlane32_swap(__float_as_uint(ps), __float_as_uint(ps), false, false); ps = __uint_as_float(rr[0]) + __uint_as_float(rr[1]); }
;     l_reg += ps;
;     ...
;     PK4(p0, 0, pa0); PK4(p0, 8, pa1); PK4(p1, 0, pa2); PK4(p1, 8, pa3);
.LBB0_605:
	v_exp_f32_e32 v96, v96
	v_exp_f32_e32 v97, v97
	v_exp_f32_e32 v98, v98
	v_exp_f32_e32 v99, v99
	v_exp_f32_e32 v100, v100
	v_exp_f32_e32 v101, v101
	v_add_f32_e32 v160, v96, v97
	v_exp_f32_e32 v102, v102
	v_add_f32_e32 v160, v98, v160
	v_exp_f32_e32 v103, v103
	v_add_f32_e32 v160, v99, v160
	v_exp_f32_e32 v104, v104
	v_add_f32_e32 v160, v100, v160
	v_exp_f32_e32 v105, v105
	v_add_f32_e32 v160, v101, v160
	v_exp_f32_e32 v106, v106
	v_add_f32_e32 v160, v102, v160
	v_exp_f32_e32 v107, v107
	v_add_f32_e32 v160, v103, v160
	v_exp_f32_e32 v108, v108
	v_add_f32_e32 v160, v104, v160
	v_exp_f32_e32 v109, v109
	v_add_f32_e32 v160, v105, v160
	v_exp_f32_e32 v110, v110
	v_add_f32_e32 v160, v106, v160
	v_exp_f32_e32 v111, v111
	v_add_f32_e32 v160, v107, v160
	v_exp_f32_e32 v80, v80
	v_add_f32_e32 v160, v108, v160
	v_exp_f32_e32 v81, v81
	v_add_f32_e32 v160, v109, v160
	v_exp_f32_e32 v82, v82
	v_add_f32_e32 v160, v110, v160
	v_exp_f32_e32 v83, v83
	v_add_f32_e32 v160, v111, v160
	v_exp_f32_e32 v84, v84
	v_add_f32_e32 v160, v80, v160
	v_exp_f32_e32 v85, v85
	v_add_f32_e32 v160, v81, v160
	v_exp_f32_e32 v86, v86
	v_add_f32_e32 v160, v82, v160
	v_exp_f32_e32 v87, v87
	v_add_f32_e32 v160, v83, v160
	v_exp_f32_e32 v88, v88
	v_add_f32_e32 v160, v84, v160
	v_exp_f32_e32 v89, v89
	v_add_f32_e32 v160, v85, v160
	v_exp_f32_e32 v90, v90
	v_add_f32_e32 v160, v86, v160
	v_exp_f32_e32 v91, v91
	v_add_f32_e32 v160, v87, v160
	v_exp_f32_e32 v92, v92
	v_add_f32_e32 v160, v88, v160
	v_exp_f32_e32 v93, v93
	v_add_f32_e32 v160, v89, v160
	v_exp_f32_e32 v94, v94
	v_add_f32_e32 v160, v90, v160
	v_exp_f32_e32 v95, v95
	v_add_f32_e32 v160, v91, v160
	v_add_f32_e32 v160, v92, v160
	v_add_f32_e32 v160, v93, v160
	v_add_f32_e32 v160, v94, v160
	v_add_f32_e32 v160, v95, v160
	v_mov_b32_e32 v161, v160
	v_cvt_pk_bf16_f32 v172, v96, v97
	v_cvt_pk_bf16_f32 v173, v98, v99
	v_permlane32_swap_b32_e32 v160, v161
	v_add_f32_e32 v160, v160, v161
	v_add_f32_e32 v204, v204, v160
	v_cvt_pk_bf16_f32 v174, v100, v101
	v_cvt_pk_bf16_f32 v175, v102, v103
	v_cvt_pk_bf16_f32 v168, v104, v105
	v_cvt_pk_bf16_f32 v169, v106, v107
	v_cvt_pk_bf16_f32 v170, v108, v109
	v_cvt_pk_bf16_f32 v171, v110, v111
	v_cvt_pk_bf16_f32 v164, v80, v81
	v_cvt_pk_bf16_f32 v165, v82, v83
	v_cvt_pk_bf16_f32 v166, v84, v85
	v_cvt_pk_bf16_f32 v167, v86, v87
	v_cvt_pk_bf16_f32 v160, v88, v89
	v_cvt_pk_bf16_f32 v161, v90, v91
	v_cvt_pk_bf16_f32 v162, v92, v93
	v_cvt_pk_bf16_f32 v163, v94, v95
	s_mul_i32 s47, s26, 0x6000
	s_addk_i32 s93, 0xc000
	s_cmp_lg_u32 s26, 0
	s_cselect_b32 s46, s93, 0x8000
	v_add_u32_e32 v227, s46, v202
	s_waitcnt lgkmcnt(0)
	ds_read_b64_tr_b16 v[208:209], v227 offset:0
	ds_read_b64_tr_b16 v[210:211], v227 offset:2048
	ds_read_b64_tr_b16 v[212:213], v227 offset:512
	ds_read_b64_tr_b16 v[214:215], v227 offset:2560
	s_barrier
; template <int DQK, bool HASQK, bool HASPV, int J>
; __device__ __forceinline__ void slot_read(bf16x8 (&kf)[DQK / 16][2], s16x4 (&vf)[4][8], const int (&ka_)[4], int vb_) {
;     constexpr int NQS = HASQK ? 2 * (DQK / 16) : 0, NS = NQS + (HASPV ? 16 : 0);
;     if constexpr (J < NQS) { constexpr int d0 = J >> 1, h = J & 1; dsr128<(d0 >> 2) * 128 + h * 32 * DQK * 2>(kf[d0][h], ka_[d0 & 3]); }
;     else if constexpr (J < NS) { constexpr int q = J - NQS, g = q >> 2, d = q & 3; dstr64<v_rd_off(d, g, 0)>(vf[g][2 * d], vb_); dstr64<v_rd_off(d, g, 1)>(vf[g][2 * d + 1], vb_); }
; }
; template <int DQK, bool HASQK, bool HASPV, int J> ...
;     constexpr int NQS = HASQK ? 2 * (DQK / 16) : 0, NS = NQS + (HASPV ? 16 : 0);
;     if constexpr (J < NS) {
;         constexpr int rd1 = (J + 1 < NS) ? ((J + 1 < NQS) ? 1 : 2) : 0, rd2 = (J + 2 < NS) ? ((J + 2 < NQS) ? 1 : 2) : 0, rd3 = (J + 3 < NS) ? ((J + 3 < NQS) ? 1 : 2) : 0, NW = rd1 + rd2 + rd3;
;     ...
;         if constexpr (J < NQS) { constexpr int d0 = J >> 1, h = J & 1;
;             LWN1(kf[d0][h]); SBAR();
;             if constexpr (h == 0) p0 = __builtin_amdgcn_mfma_f32_32x32x16_bf16(kf[d0][0], qr[d0], (d0 == 0) ? negm : p0, 0, 0, 0);
;             else p1 = __builtin_amdgcn_mfma_f32_32x32x16_bf16(kf[d0][1], qr[d0], (d0 == 0) ? negm : p1, 0, 0, 0);
;         } else { constexpr int q = J - NQS, g = q >> 2, d = q & 3;
;             LWN2(vf[g][2 * d], vf[g][2 * d + 1]); SBAR();
;             o[d] = __builtin_amdgcn_mfma_f32_32x32x16_bf16(pa[g], (bf16x8){vf[g][2 * d][0], vf[g][2 * d][1], vf[g][2 * d][2], vf[g][2 * d][3], vf[g][2 * d + 1][0], vf[g][2 * d + 1][1], vf[g][2 * d + 1][2], vf[g][2 * d + 1][3]}, o[d], 0, 0, 0);
;         }
;     ...
;         SBAR();
;         slot_read<DQK, HASQK, HASPV, J + 4>(kf, vf, ka_, vb_);
;         SBAR();
;         slot_run<DQK, HASQK, HASPV, J + 1>(kf, vf, ka_, vb_, qr, p0, p1, negm, o, pa);
;     }
; }
;     ...
;     for (int i = 0; i < NT - 1; ++i) {
;         SEG_S(i);
;         { const int cp = (ci == 0) ? 2 : ci - 1, cn = (ci == 2) ? 0 : ci + 1;
;           if (DMA_M) { if (i + 3 < NT) DMA_K(i + 3, cp); if (i + 2 < NT) DMA_V(i + 2, cn); }
;           SEG_M(true, true, ci, cp);
;           if (DMA_M && i + 3 < NT) asm volatile("s_waitcnt vmcnt(%0)" :: "n"(NKW + 2) : "memory");
;           else asm volatile("s_waitcnt vmcnt(0)" ::: "memory");
;           BAR_ALL(); }
	ds_read_b64_tr_b16 v[216:217], v227 offset:1024
	ds_read_b64_tr_b16 v[218:219], v227 offset:3072
	ds_read_b64_tr_b16 v[220:221], v227 offset:1536
	ds_read_b64_tr_b16 v[222:223], v227 offset:3584
	s_waitcnt lgkmcnt(6)
	v_mfma_f32_32x32x16_bf16 v[64:79], v[172:175], v[208:211], v[64:79]
	ds_read_b64_tr_b16 v[208:209], v227 offset:4096
	ds_read_b64_tr_b16 v[210:211], v227 offset:6144
	v_add_u32_e32 v207, s47, v185
	s_waitcnt lgkmcnt(6)
	v_mfma_f32_32x32x16_bf16 v[48:63], v[172:175], v[212:215], v[48:63]
	ds_read_b64_tr_b16 v[212:213], v227 offset:4608
	ds_read_b64_tr_b16 v[214:215], v227 offset:6656
	v_add_u32_e32 v224, s47, v187
	s_waitcnt lgkmcnt(6)
	v_mfma_f32_32x32x16_bf16 v[32:47], v[172:175], v[216:219], v[32:47]
	ds_read_b64_tr_b16 v[216:217], v227 offset:5120
	ds_read_b64_tr_b16 v[218:219], v227 offset:7168
	v_add_u32_e32 v225, s47, v205
	s_waitcnt lgkmcnt(6)
	v_mfma_f32_32x32x16_bf16 v[16:31], v[172:175], v[220:223], v[16:31]
	ds_read_b64_tr_b16 v[220:221], v227 offset:5632
	ds_read_b64_tr_b16 v[222:223], v227 offset:7680
	v_add_u32_e32 v226, s47, v206
	s_waitcnt lgkmcnt(6)
	v_mfma_f32_32x32x16_bf16 v[64:79], v[168:171], v[208:211], v[64:79]
	ds_read_b64_tr_b16 v[208:209], v227 offset:8192
	ds_read_b64_tr_b16 v[210:211], v227 offset:10240
	s_waitcnt lgkmcnt(6)
	v_mfma_f32_32x32x16_bf16 v[48:63], v[168:171], v[212:215], v[48:63]
	ds_read_b64_tr_b16 v[212:213], v227 offset:8704
	ds_read_b64_tr_b16 v[214:215], v227 offset:10752
	s_waitcnt lgkmcnt(6)
	v_mfma_f32_32x32x16_bf16 v[32:47], v[168:171], v[216:219], v[32:47]
	ds_read_b64_tr_b16 v[216:217], v227 offset:9216
	ds_read_b64_tr_b16 v[218:219], v227 offset:11264
	s_waitcnt lgkmcnt(6)
	v_mfma_f32_32x32x16_bf16 v[16:31], v[168:171], v[220:223], v[16:31]
	ds_read_b64_tr_b16 v[220:221], v227 offset:9728
	ds_read_b64_tr_b16 v[222:223], v227 offset:11776
	s_waitcnt lgkmcnt(6)
	v_mfma_f32_32x32x16_bf16 v[64:79], v[164:167], v[208:211], v[64:79]
	ds_read_b64_tr_b16 v[208:209], v227 offset:12288
	ds_read_b64_tr_b16 v[210:211], v227 offset:14336
	s_waitcnt lgkmcnt(6)
	v_mfma_f32_32x32x16_bf16 v[48:63], v[164:167], v[212:215], v[48:63]
	ds_read_b64_tr_b16 v[212:213], v227 offset:12800
	ds_read_b64_tr_b16 v[214:215], v227 offset:14848
	s_waitcnt lgkmcnt(6)
	v_mfma_f32_32x32x16_bf16 v[32:47], v[164:167], v[216:219], v[32:47]
	ds_read_b64_tr_b16 v[216:217], v227 offset:13312
	ds_read_b64_tr_b16 v[218:219], v227 offset:15360
	s_waitcnt lgkmcnt(6)
	v_mfma_f32_32x32x16_bf16 v[16:31], v[164:167], v[220:223], v[16:31]
	ds_read_b64_tr_b16 v[220:221], v227 offset:13824
	ds_read_b64_tr_b16 v[222:223], v227 offset:15872
	v_xor_b32_e32 v80, 0x80000000, v203
	v_mov_b32_e32 v81, v80
	v_mov_b32_e32 v82, v80
	v_mov_b32_e32 v83, v80
	v_mov_b32_e32 v84, v80
	v_mov_b32_e32 v85, v80
	v_mov_b32_e32 v86, v80
	v_mov_b32_e32 v87, v80
	v_mov_b32_e32 v88, v80
	v_mov_b32_e32 v89, v80
	v_mov_b32_e32 v90, v80
	v_mov_b32_e32 v91, v80
	v_mov_b32_e32 v92, v80
	v_mov_b32_e32 v93, v80
	v_mov_b32_e32 v94, v80
	v_mov_b32_e32 v95, v80
	s_waitcnt lgkmcnt(6)
	v_mfma_f32_32x32x16_bf16 v[64:79], v[160:163], v[208:211], v[64:79]
	ds_read_b128 v[208:211], v207 offset:0
	s_waitcnt lgkmcnt(5)
	v_mfma_f32_32x32x16_bf16 v[48:63], v[160:163], v[212:215], v[48:63]
	ds_read_b128 v[212:215], v207 offset:12288
	s_waitcnt lgkmcnt(4)
	v_mfma_f32_32x32x16_bf16 v[32:47], v[160:163], v[216:219], v[32:47]
	ds_read_b128 v[216:219], v224 offset:0
	s_waitcnt lgkmcnt(3)
	v_mfma_f32_32x32x16_bf16 v[16:31], v[160:163], v[220:223], v[16:31]
	ds_read_b128 v[220:223], v224 offset:12288
	s_waitcnt lgkmcnt(3)
	v_mfma_f32_32x32x16_bf16 v[96:111], v[208:211], v[112:115], v[80:95]
	ds_read_b128 v[208:211], v225 offset:0
	s_waitcnt lgkmcnt(3)
	v_mfma_f32_32x32x16_bf16 v[80:95], v[212:215], v[112:115], v[80:95]
	ds_read_b128 v[212:215], v225 offset:12288
	s_waitcnt lgkmcnt(3)
	v_mfma_f32_32x32x16_bf16 v[96:111], v[216:219], v[116:119], v[96:111]
	ds_read_b128 v[216:219], v226 offset:0
	s_waitcnt lgkmcnt(3)
	v_mfma_f32_32x32x16_bf16 v[80:95], v[220:223], v[116:119], v[80:95]
	ds_read_b128 v[220:223], v226 offset:12288
	s_waitcnt lgkmcnt(3)
	v_mfma_f32_32x32x16_bf16 v[96:111], v[208:211], v[120:123], v[96:111]
	ds_read_b128 v[208:211], v207 offset:128
	s_waitcnt lgkmcnt(3)
	v_mfma_f32_32x32x16_bf16 v[80:95], v[212:215], v[120:123], v[80:95]
	ds_read_b128 v[212:215], v207 offset:12416
	s_waitcnt lgkmcnt(3)
	v_mfma_f32_32x32x16_bf16 v[96:111], v[216:219], v[124:127], v[96:111]
	ds_read_b128 v[216:219], v224 offset:128
	s_waitcnt lgkmcnt(3)
	v_mfma_f32_32x32x16_bf16 v[80:95], v[220:223], v[124:127], v[80:95]
	ds_read_b128 v[220:223], v224 offset:12416
	s_waitcnt lgkmcnt(3)
	v_mfma_f32_32x32x16_bf16 v[96:111], v[208:211], v[128:131], v[96:111]
	ds_read_b128 v[208:211], v225 offset:128
	s_waitcnt lgkmcnt(3)
	v_mfma_f32_32x32x16_bf16 v[80:95], v[212:215], v[128:131], v[80:95]
	ds_read_b128 v[212:215], v225 offset:12416
	s_waitcnt lgkmcnt(3)
	v_mfma_f32_32x32x16_bf16 v[96:111], v[216:219], v[132:135], v[96:111]
	ds_read_b128 v[216:219], v226 offset:128
	s_waitcnt lgkmcnt(3)
	v_mfma_f32_32x32x16_bf16 v[80:95], v[220:223], v[132:135], v[80:95]
	ds_read_b128 v[220:223], v226 offset:12416
	s_waitcnt lgkmcnt(3)
	v_mfma_f32_32x32x16_bf16 v[96:111], v[208:211], v[136:139], v[96:111]
	ds_read_b128 v[208:211], v207 offset:256
	s_waitcnt lgkmcnt(3)
	v_mfma_f32_32x32x16_bf16 v[80:95], v[212:215], v[136:139], v[80:95]
	ds_read_b128 v[212:215], v207 offset:12544
	s_waitcnt lgkmcnt(3)
	v_mfma_f32_32x32x16_bf16 v[96:111], v[216:219], v[140:143], v[96:111]
	ds_read_b128 v[216:219], v224 offset:256
	s_waitcnt lgkmcnt(3)
	v_mfma_f32_32x32x16_bf16 v[80:95], v[220:223], v[140:143], v[80:95]
	ds_read_b128 v[220:223], v224 offset:12544
	s_waitcnt lgkmcnt(3)
	v_mfma_f32_32x32x16_bf16 v[96:111], v[208:211], v[144:147], v[96:111]
	ds_read_b128 v[208:211], v225 offset:256
	s_waitcnt lgkmcnt(3)
	v_mfma_f32_32x32x16_bf16 v[80:95], v[212:215], v[144:147], v[80:95]
	ds_read_b128 v[212:215], v225 offset:12544
	s_waitcnt lgkmcnt(3)
	v_mfma_f32_32x32x16_bf16 v[96:111], v[216:219], v[148:151], v[96:111]
	ds_read_b128 v[216:219], v226 offset:256
	s_waitcnt lgkmcnt(3)
	v_mfma_f32_32x32x16_bf16 v[80:95], v[220:223], v[148:151], v[80:95]
	ds_read_b128 v[220:223], v226 offset:12544
	s_waitcnt lgkmcnt(3)
	v_mfma_f32_32x32x16_bf16 v[96:111], v[208:211], v[152:155], v[96:111]
	s_waitcnt lgkmcnt(2)
	v_mfma_f32_32x32x16_bf16 v[80:95], v[212:215], v[152:155], v[80:95]
	s_waitcnt lgkmcnt(1)
	v_mfma_f32_32x32x16_bf16 v[96:111], v[216:219], v[156:159], v[96:111]
	s_waitcnt lgkmcnt(0)
	v_mfma_f32_32x32x16_bf16 v[80:95], v[220:223], v[156:159], v[80:95]
	s_waitcnt vmcnt(0)
	s_waitcnt lgkmcnt(0)
	s_barrier
	s_add_u32 s44, s44, 0x18000
	s_addc_u32 s45, s45, 0
	v_lshl_add_u64 v[194:195], v[194:195], 0, s[28:29]
	s_cmp_eq_u32 s44, 0xbe8000
	v_lshl_add_u64 v[196:197], v[196:197], 0, s[28:29]
	s_cbranch_scc1 .LBB0_616
